# short back edge no longer resets the staging state (block-major joins treat states 0 and 1 alike); the accumulator-pending flag is set once on entry from the compiled loop
# baseline (speedup 1.0000x reference)
.Lbm_back:
	s_add_i32 s11, s75, 2
	s_cmp_gt_i32 s11, s26
	s_cbranch_scc1 .LBB0_1228
	s_add_u32 s64, s64, 0x10000
	s_addc_u32 s65, s65, 0
	s_add_u32 s62, s62, 0x100
	s_addc_u32 s63, s63, 0
	v_add_u32_e32 v196, 0x200, v196
	s_addk_i32 s1, 0x4000
	s_mov_b32 s75, s11
	s_add_i32 s76, s11, 2
	s_waitcnt lgkmcnt(0)
	s_barrier
	s_branch .Lbm_step
